# v28 + static s_setprio 1 for waves 0-3 while they run the steady-state MLA loop
# speedup vs baseline: 1.0064x; 1.0064x over previous
; #define ISSUE_K(t, sl) do { glds16(Kg + (long)(t) * (KSLOT / 2), (unsigned)__builtin_amdgcn_readfirstlane(kdst + (sl) * KSLOT)); \
;         if (k2) glds16(Kg + (long)(t) * (KSLOT / 2) + 4096, (unsigned)__builtin_amdgcn_readfirstlane(kdst + (sl) * KSLOT + 8192)); } while (0)
; #define ISSUE_V(t, sl) glds16(Vg + (long)(t) * 4096, (unsigned)__builtin_amdgcn_readfirstlane(vdst + (sl) * VSLOT))
; #define SFENCE() __builtin_amdgcn_sched_barrier(0)
; template <bool FOX>
; __device__ __forceinline__ void attn_unit(const Args& A, int b, int h, int qb, LAS char* shm, LAS float* dg) {
;     ...
;     for (int t = 1; t < t_end; ++t) {
;         if (t == 1 && 4 < nti) ISSUE_K(t0 + 4, 0);
;         if (t + 4 < nti) ISSUE_K(t0 + t + 4, t % NS);
;         if (t + 2 < nti) ISSUE_V(t0 + t + 2, (t + 2) % NS);
;         SFENCE();
.LBB0_825:
	s_add_i32 s27, s26, 3
	s_cmp_lt_u32 s27, s94
	s_cbranch_scc0 .LBB0_828
	s_cmp_lg_u32 s98, 0
	s_cbranch_scc0 .Lmla_ss_no
	s_cmp_lg_u32 s26, s59
	s_cbranch_scc0 .Lmla_ss_no
	s_and_b32 s52, s27, 3
	s_mulk_i32 s52, 0x3000
	s_add_i32 s52, s52, s91
	s_add_i32 s53, s42, 0x6000
	s_and_b32 s53, s53, 0x6000
	s_add_i32 s53, s53, s93
	v_lshl_add_u64 v[250:251], v[232:233], 0, s[42:43]
	v_lshl_add_u64 v[240:241], v[234:235], 0, s[56:57]
	s_cmp_lt_i32 s89, 4
	s_cbranch_scc0 .Lmla_ss2_top
	s_setprio 1
	s_branch .Lmla_ss1_in
